# speedup vs baseline: 1.0035x; 1.0016x over previous
.LBB2_355:
	s_or_b64 exec, exec, s[52:53]
	s_add_u32 s52, s92, 0x80
	s_addc_u32 s53, s93, 0
	s_add_i32 s82, 0, 0x18000
	s_add_i32 s58, s82, s57
	s_waitcnt vmcnt(8)
	v_mfma_f32_16x16x32_f16 v[102:105], v[30:33], v[6:9], 0
	s_mov_b32 m0, s58
	s_waitcnt vmcnt(4)
	v_lshl_add_u32 v248, v149, 4, v152
	v_lshlrev_b32_e32 v248, 2, v248
	v_add_u32_e32 v248, 0x20000, v248
	ds_write_b32 v248, v246
	ds_write_b32 v248, v247 offset:512
	s_barrier
	v_mfma_f32_16x16x32_f16 v[98:101], v[26:29], v[6:9], 0
	v_mfma_f32_16x16x32_f16 v[126:129], v[30:33], v[2:5], 0
	v_mfma_f32_16x16x32_f16 v[122:125], v[26:29], v[2:5], 0
	v_mfma_f32_16x16x32_f16 v[118:121], v[30:33], v[14:17], 0
	v_mfma_f32_16x16x32_f16 v[110:113], v[30:33], v[10:13], 0
	v_mfma_f32_16x16x32_f16 v[94:97], v[142:145], v[6:9], 0
	v_mfma_f32_16x16x32_f16 v[90:93], v[138:141], v[6:9], 0
	v_mfma_f32_16x16x32_f16 v[86:89], v[142:145], v[2:5], 0
	v_mfma_f32_16x16x32_f16 v[82:85], v[138:141], v[2:5], 0
	v_mfma_f32_16x16x32_f16 v[62:65], v[30:33], v[22:25], 0
	v_mfma_f32_16x16x32_f16 v[54:57], v[30:33], v[18:21], 0
	v_mfma_f32_16x16x32_f16 v[46:49], v[30:33], v[134:137], 0
	v_mfma_f32_16x16x32_f16 v[38:41], v[30:33], v[130:133], 0
	v_mfma_f32_16x16x32_f16 v[30:33], v[26:29], v[130:133], 0
	v_mfma_f32_16x16x32_f16 v[6:9], v[142:145], v[130:133], 0
	v_mfma_f32_16x16x32_f16 v[2:5], v[138:141], v[130:133], 0
	v_lshl_add_u64 v[130:131], s[52:53], 0, v[162:163]
	s_add_u32 s52, s52, 0x20000
	global_load_lds_dwordx4 v[130:131], off
	s_addc_u32 s53, s53, 0
	s_add_i32 m0, s58, 0x2000
	s_add_u32 s58, s90, 0x80
	s_addc_u32 s59, s91, 0
	v_lshl_add_u64 v[130:131], s[52:53], 0, v[162:163]
	s_add_i32 s52, s97, 0x8000
	global_load_lds_dwordx4 v[130:131], off
	v_lshl_add_u64 v[130:131], s[58:59], 0, v[162:163]
	s_add_u32 s58, s58, 0x20000
	s_addc_u32 s59, s59, 0
	s_mov_b32 m0, s52
	s_add_i32 s53, s97, 0xa000
	global_load_lds_dwordx4 v[130:131], off
	v_lshl_add_u64 v[130:131], s[58:59], 0, v[162:163]
	s_add_u32 s58, s92, 0x40080
	s_addc_u32 s59, s93, 0
	s_add_i32 s83, 0, 0x1c000
	s_mov_b32 m0, s53
	s_add_i32 s57, s83, s57
	global_load_lds_dwordx4 v[130:131], off
	v_lshl_add_u64 v[130:131], s[58:59], 0, v[162:163]
	s_add_u32 s58, s58, 0x20000
	s_mov_b32 m0, s57
	s_addc_u32 s59, s59, 0
	global_load_lds_dwordx4 v[130:131], off
	s_add_i32 m0, s57, 0x2000
	v_lshl_add_u64 v[130:131], s[58:59], 0, v[162:163]
	global_load_lds_dwordx4 v[130:131], off
	v_lshlrev_b32_e32 v132, 2, v152
	v_lshlrev_b32_e32 v130, 6, v152
	v_and_b32_e32 v131, 32, v132
	v_bitop3_b32 v130, v130, v131, v146 bitop3:0x36
	s_add_i32 s57, 0, 0x10000
	v_add_u32_e32 v131, s57, v130
	s_add_i32 s57, 0, 0x14000
	v_mfma_f32_16x16x32_f16 v[114:117], v[26:29], v[14:17], 0
	s_waitcnt vmcnt(6)
	v_lshlrev_b32_e32 v133, 13, v154
	s_barrier
	v_mfma_f32_16x16x32_f16 v[106:109], v[26:29], v[10:13], 0
	v_mfma_f32_16x16x32_f16 v[78:81], v[142:145], v[14:17], 0
	v_mfma_f32_16x16x32_f16 v[74:77], v[138:141], v[14:17], 0
	v_mfma_f32_16x16x32_f16 v[70:73], v[142:145], v[10:13], 0
	v_mfma_f32_16x16x32_f16 v[66:69], v[138:141], v[10:13], 0
	v_mfma_f32_16x16x32_f16 v[58:61], v[26:29], v[22:25], 0
	v_mfma_f32_16x16x32_f16 v[50:53], v[26:29], v[18:21], 0
	v_mfma_f32_16x16x32_f16 v[42:45], v[26:29], v[134:137], 0
	v_mfma_f32_16x16x32_f16 v[34:37], v[142:145], v[22:25], 0
	v_mfma_f32_16x16x32_f16 v[26:29], v[138:141], v[22:25], 0
	v_mfma_f32_16x16x32_f16 v[22:25], v[142:145], v[18:21], 0
	v_mfma_f32_16x16x32_f16 v[18:21], v[138:141], v[18:21], 0
	v_mfma_f32_16x16x32_f16 v[14:17], v[142:145], v[134:137], 0
	v_mfma_f32_16x16x32_f16 v[10:13], v[138:141], v[134:137], 0
	v_add_u32_e32 v136, s57, v130
	v_add_u32_e32 v139, s82, v130
	v_add_u32_e32 v140, s83, v130
	v_or_b32_e32 v130, v151, v152
	v_lshlrev_b32_e32 v134, 6, v130
	s_movk_i32 s57, 0x3c0
	v_lshlrev_b32_e32 v130, 2, v130
	v_and_or_b32 v134, v134, s57, v146
	v_and_b32_e32 v130, 32, v130
	v_xad_u32 v130, v134, v130, 0
	v_or_b32_e32 v134, 16, v151
	v_or_b32_e32 v137, v134, v152
	v_lshlrev_b32_e32 v138, 6, v137
	v_lshlrev_b32_e32 v137, 2, v137
	v_and_or_b32 v138, v138, s57, v146
	v_and_b32_e32 v137, 32, v137
	v_lshlrev_b32_e32 v141, 7, v134
	v_or_b32_e32 v134, 32, v151
	v_xad_u32 v137, v138, v137, 0
	v_or_b32_e32 v138, v134, v152
	v_lshlrev_b32_e32 v142, 6, v138
	v_lshlrev_b32_e32 v138, 2, v138
	v_and_or_b32 v142, v142, s57, v146
	v_and_b32_e32 v138, 32, v138
	v_lshlrev_b32_e32 v143, 7, v134
	v_or_b32_e32 v134, 48, v151
	v_xad_u32 v142, v142, v138, 0
	v_or_b32_e32 v138, v134, v152
	v_lshlrev_b32_e32 v144, 6, v138
	v_lshlrev_b32_e32 v138, 2, v138
	v_and_or_b32 v144, v144, s57, v146
	v_and_b32_e32 v138, 32, v138
	v_lshlrev_b32_e32 v135, 12, v153
	v_xad_u32 v144, v144, v138, 0
	v_lshlrev_b32_e32 v145, 7, v134
	s_mov_b32 s57, 0
	v_add_u32_e32 v138, v131, v135
	v_add_u32_e32 v134, v130, v133
	v_add_u32_e32 v133, v137, v141
	v_add_u32_e32 v131, v142, v143
	v_add_u32_e32 v130, v144, v145
	v_add_u32_e32 v137, v136, v135
	v_add_u32_e32 v136, v139, v135
	v_add_u32_e32 v135, v140, v135
	s_cmp_ge_u32 s97, 0x1000
	s_cbranch_scc1 .Lg2_prio_done
	s_setprio 1
.Lg2_prio_done:
	s_cmp_lg_u32 s100, 0
	s_cbranch_scc1 .Lg2p_loop
	s_branch .LBB2_356

.LBB2_381:
	s_or_b64 exec, exec, s[34:35]
	s_add_u32 s34, s4, 0x80
	s_addc_u32 s35, s5, 0
	s_add_i32 s58, 0, 0x18000
	s_add_i32 s56, s58, s33
	v_lshl_add_u64 v[4:5], s[34:35], 0, v[162:163]
	s_add_u32 s34, s34, 0x40000
	s_mov_b32 m0, s56
	s_addc_u32 s35, s35, 0
	s_waitcnt vmcnt(4)
	s_barrier
	global_load_lds_dwordx4 v[4:5], off
	s_add_i32 m0, s56, 0x2000
	v_readlane_b32 s56, v244, 6
	v_mov_b32_e32 v135, v163
	v_lshl_add_u64 v[4:5], s[34:35], 0, v[162:163]
	v_readlane_b32 s57, v244, 7
	s_add_i32 s34, s52, 0x8000
	v_mov_b32_e32 v137, v163
	global_load_lds_dwordx4 v[4:5], off
	s_mov_b32 m0, s34
	v_lshl_add_u64 v[4:5], s[56:57], 0, v[134:135]
	s_add_i32 s35, s52, 0xa000
	global_load_lds_dwordx4 v[4:5], off
	v_lshl_add_u64 v[4:5], s[56:57], 0, v[136:137]
	s_add_u32 s56, s4, 0x80080
	s_addc_u32 s57, s5, 0
	s_add_i32 s59, 0, 0x1c000
	s_mov_b32 m0, s35
	s_add_i32 s33, s59, s33
	global_load_lds_dwordx4 v[4:5], off
	v_lshl_add_u64 v[4:5], s[56:57], 0, v[162:163]
	s_add_u32 s56, s56, 0x40000
	s_mov_b32 m0, s33
	s_addc_u32 s57, s57, 0
	global_load_lds_dwordx4 v[4:5], off
	s_add_i32 m0, s33, 0x2000
	v_lshl_add_u64 v[4:5], s[56:57], 0, v[162:163]
	global_load_lds_dwordx4 v[4:5], off
	v_and_b32_e32 v139, 15, v141
	v_bfe_u32 v140, v141, 4, 2
	v_lshlrev_b32_e32 v6, 2, v141
	v_lshlrev_b32_e32 v4, 4, v140
	v_lshlrev_b32_e32 v5, 6, v139
	v_and_b32_e32 v6, 32, v6
	v_bitop3_b32 v5, v4, v6, v5 bitop3:0x36
	s_add_i32 s33, 0, 0x10000
	v_add_u32_e32 v7, s33, v5
	s_add_i32 s33, 0, 0x14000
	v_lshlrev_b32_e32 v143, 6, v2
	v_add_u32_e32 v8, s33, v5
	v_lshlrev_b32_e32 v11, 13, v2
	v_lshlrev_b32_e32 v2, 6, v141
	s_movk_i32 s33, 0x3c0
	v_and_b32_e32 v142, 3, v138
	s_waitcnt vmcnt(6)
	v_and_or_b32 v2, v2, s33, v4
	v_lshlrev_b32_e32 v3, 12, v142
	v_add_u32_e32 v9, s58, v5
	v_add_u32_e32 v10, s59, v5
	v_add_u32_e32 v5, 0, v5
	v_xad_u32 v4, v2, v6, 0
	v_or_b32_e32 v6, 0x800, v11
	v_or_b32_e32 v12, 0x1000, v11
	v_or_b32_e32 v13, 0x1800, v11
	v_mov_b32_e32 v2, 0
	s_mov_b32 s84, 0
	v_add_u32_e32 v151, v7, v3
	v_add_u32_e32 v147, v5, v11
	v_add_u32_e32 v146, v4, v6
	v_add_u32_e32 v145, v4, v12
	v_add_u32_e32 v144, v4, v13
	v_add_u32_e32 v150, v8, v3
	v_add_u32_e32 v149, v9, v3
	v_add_u32_e32 v148, v10, v3
	v_mov_b32_e32 v3, v2
	v_mov_b32_e32 v4, v2
	v_mov_b32_e32 v5, v2
	v_mov_b32_e32 v6, v2
	v_mov_b32_e32 v7, v2
	v_mov_b32_e32 v8, v2
	v_mov_b32_e32 v9, v2
	v_mov_b32_e32 v10, v2
	v_mov_b32_e32 v11, v2
	v_mov_b32_e32 v12, v2
	v_mov_b32_e32 v13, v2
	v_mov_b32_e32 v14, v2
	v_mov_b32_e32 v15, v2
	v_mov_b32_e32 v16, v2
	v_mov_b32_e32 v17, v2
	v_mov_b32_e32 v18, v2
	v_mov_b32_e32 v19, v2
	v_mov_b32_e32 v20, v2
	v_mov_b32_e32 v21, v2
	v_mov_b32_e32 v22, v2
	v_mov_b32_e32 v23, v2
	v_mov_b32_e32 v24, v2
	v_mov_b32_e32 v25, v2
	v_mov_b32_e32 v26, v2
	v_mov_b32_e32 v27, v2
	v_mov_b32_e32 v28, v2
	v_mov_b32_e32 v29, v2
	v_mov_b32_e32 v30, v2
	v_mov_b32_e32 v31, v2
	v_mov_b32_e32 v32, v2
	v_mov_b32_e32 v33, v2
	v_mov_b32_e32 v34, v2
	v_mov_b32_e32 v35, v2
	v_mov_b32_e32 v36, v2
	v_mov_b32_e32 v37, v2
	v_mov_b32_e32 v38, v2
	v_mov_b32_e32 v39, v2
	v_mov_b32_e32 v40, v2
	v_mov_b32_e32 v41, v2
	v_mov_b32_e32 v42, v2
	v_mov_b32_e32 v43, v2
	v_mov_b32_e32 v44, v2
	v_mov_b32_e32 v45, v2
	v_mov_b32_e32 v46, v2
	v_mov_b32_e32 v47, v2
	v_mov_b32_e32 v48, v2
	v_mov_b32_e32 v49, v2
	v_mov_b32_e32 v50, v2
	v_mov_b32_e32 v51, v2
	v_mov_b32_e32 v52, v2
	v_mov_b32_e32 v53, v2
	v_mov_b32_e32 v54, v2
	v_mov_b32_e32 v55, v2
	v_mov_b32_e32 v56, v2
	v_mov_b32_e32 v57, v2
	v_mov_b32_e32 v58, v2
	v_mov_b32_e32 v59, v2
	v_mov_b32_e32 v60, v2
	v_mov_b32_e32 v61, v2
	v_mov_b32_e32 v62, v2
	v_mov_b32_e32 v63, v2
	v_mov_b32_e32 v64, v2
	v_mov_b32_e32 v65, v2
	v_mov_b32_e32 v66, v2
	v_mov_b32_e32 v67, v2
	v_mov_b32_e32 v68, v2
	v_mov_b32_e32 v69, v2
	v_mov_b32_e32 v70, v2
	v_mov_b32_e32 v71, v2
	v_mov_b32_e32 v72, v2
	v_mov_b32_e32 v73, v2
	v_mov_b32_e32 v74, v2
	v_mov_b32_e32 v75, v2
	v_mov_b32_e32 v76, v2
	v_mov_b32_e32 v77, v2
	v_mov_b32_e32 v78, v2
	v_mov_b32_e32 v79, v2
	v_mov_b32_e32 v80, v2
	v_mov_b32_e32 v81, v2
	v_mov_b32_e32 v82, v2
	v_mov_b32_e32 v83, v2
	v_mov_b32_e32 v84, v2
	v_mov_b32_e32 v85, v2
	v_mov_b32_e32 v86, v2
	v_mov_b32_e32 v87, v2
	v_mov_b32_e32 v88, v2
	v_mov_b32_e32 v89, v2
	v_mov_b32_e32 v90, v2
	v_mov_b32_e32 v91, v2
	v_mov_b32_e32 v92, v2
	v_mov_b32_e32 v93, v2
	v_mov_b32_e32 v94, v2
	v_mov_b32_e32 v95, v2
	v_mov_b32_e32 v96, v2
	v_mov_b32_e32 v97, v2
	v_mov_b32_e32 v98, v2
	v_mov_b32_e32 v99, v2
	v_mov_b32_e32 v100, v2
	v_mov_b32_e32 v101, v2
	v_mov_b32_e32 v102, v2
	v_mov_b32_e32 v103, v2
	v_mov_b32_e32 v104, v2
	v_mov_b32_e32 v105, v2
	v_mov_b32_e32 v106, v2
	v_mov_b32_e32 v107, v2
	v_mov_b32_e32 v108, v2
	v_mov_b32_e32 v109, v2
	v_mov_b32_e32 v110, v2
	v_mov_b32_e32 v111, v2
	v_mov_b32_e32 v112, v2
	v_mov_b32_e32 v113, v2
	v_mov_b32_e32 v114, v2
	v_mov_b32_e32 v115, v2
	v_mov_b32_e32 v116, v2
	v_mov_b32_e32 v117, v2
	v_mov_b32_e32 v118, v2
	v_mov_b32_e32 v119, v2
	v_mov_b32_e32 v120, v2
	v_mov_b32_e32 v121, v2
	v_mov_b32_e32 v122, v2
	v_mov_b32_e32 v123, v2
	v_mov_b32_e32 v124, v2
	v_mov_b32_e32 v125, v2
	v_mov_b32_e32 v126, v2
	v_mov_b32_e32 v127, v2
	v_mov_b32_e32 v128, v2
	v_mov_b32_e32 v129, v2
	v_mov_b32_e32 v133, v163
	v_mov_b32_e32 v131, v163
	s_barrier
	s_cmp_ge_u32 s52, 0x1000
	s_cbranch_scc1 .Lg1_prio_done
	s_setprio 1
